# attention halves: runs of lgkmcnt waits with no LDS issue between them merged into one stricter wait (fewer issue slots)
# baseline (speedup 1.0000x reference)
; template <int OFF> DEVI s16x4 tr_read(int vb) { s16x4 r; asm volatile("ds_read_b64_tr_b16 %0, %1 offset:%2" : "=&v"(r) : "v"(vb), "i"(OFF) : "memory"); return r; }
; DEVI void pv_both(f32x16& o0, f32x16& o1, int vb, bf16x8 pa0, bf16x8 pa1, bf16x8 pa2, bf16x8 pa3) {
;     const s16x4 a0 = tr_read<v_rd_off(0, 0, 0)>(vb), b0 = tr_read<v_rd_off(0, 0, 1)>(vb), a1 = tr_read<v_rd_off(0, 1, 0)>(vb), b1 = tr_read<v_rd_off(0, 1, 1)>(vb);
;     const s16x4 a2 = tr_read<v_rd_off(0, 2, 0)>(vb), b2 = tr_read<v_rd_off(0, 2, 1)>(vb), a3 = tr_read<v_rd_off(0, 3, 0)>(vb), b3 = tr_read<v_rd_off(0, 3, 1)>(vb);
;     const s16x4 c0 = tr_read<v_rd_off(1, 0, 0)>(vb), d0 = tr_read<v_rd_off(1, 0, 1)>(vb), c1 = tr_read<v_rd_off(1, 1, 0)>(vb), d1 = tr_read<v_rd_off(1, 1, 1)>(vb);
;     const s16x4 c2 = tr_read<v_rd_off(1, 2, 0)>(vb), d2 = tr_read<v_rd_off(1, 2, 1)>(vb), c3 = tr_read<v_rd_off(1, 3, 0)>(vb), d3 = tr_read<v_rd_off(1, 3, 1)>(vb);
; DEVI void finishSM(f32x16& p0, f32x16& p1, float alpha, float& l_reg, bf16x8& pa0, bf16x8& pa1, bf16x8& pa2, bf16x8& pa3) {
; #pragma unroll
;     for (int r = 0; r < 16; ++r) p1[r] = __builtin_amdgcn_exp2f(p1[r]);
;     f32x2 s2 = (f32x2){p0[0], p0[1]} + (f32x2){p1[0], p1[1]};
; #pragma unroll
;     for (int r = 2; r < 16; r += 2) s2 += (f32x2){p0[r], p0[r + 1]} + (f32x2){p1[r], p1[r + 1]};
;     float ps = s2[0] + s2[1];
;     { auto rr = __builtin_amdgcn_permlane32_swap(__float_as_uint(ps), __float_as_uint(ps), false, false);
;       ps = __uint_as_float(rr[0]) + __uint_as_float(rr[1]); }
;     l_reg = l_reg * alpha + ps;
;     ...
;     PK4(p0, 0, pa0); PK4(p0, 8, pa1); PK4(p1, 0, pa2); PK4(p1, 8, pa3);
;     ...
; }
; DEVI void qkt(f32x16& p0, f32x16& p1, const char* Kb, const bf16x8 (&qr)[6], int r32, int hi, const f32x16& cinit) {
; #pragma unroll
;     for (int d0 = 0; d0 < 6; ++d0) { const int cb = (d0 * 16 + hi * 8) * 2;
;         const bf16x8 k0 = *(const bf16x8*)(Kb + KSWZ(r32, cb)), k1 = *(const bf16x8*)(Kb + KSWZ(32 + r32, cb));
;         p0 = __builtin_amdgcn_mfma_f32_32x32x16_bf16(k0, qr[d0], d0 == 0 ? cinit : p0, 0, 0, 0);
;         p1 = __builtin_amdgcn_mfma_f32_32x32x16_bf16(k1, qr[d0], d0 == 0 ? cinit : p1, 0, 0, 0); }
.LBB0_696:
	v_add_u32_e32 v174, s98, v204
	v_exp_f32_e32 v66, v66
	v_exp_f32_e32 v67, v67
	s_waitcnt lgkmcnt(1)
	v_mfma_f32_32x32x16_bf16 v[98:113], v[82:85], v[150:153], v[34:49]
	v_add_u32_e32 v82, s98, v184
	v_add_u32_e32 v83, s98, v185
	ds_read_b128 v[208:211], v82 offset:12288
	ds_read_b128 v[212:215], v82 offset:18432
	ds_read_b128 v[216:219], v83 offset:12288
	ds_read_b128 v[220:223], v83 offset:18432
	v_exp_f32_e32 v68, v68
	v_exp_f32_e32 v69, v69
	v_exp_f32_e32 v70, v70
	v_exp_f32_e32 v71, v71
	s_waitcnt lgkmcnt(4)
	v_mfma_f32_32x32x16_bf16 v[82:97], v[124:127], v[150:153], v[34:49]
	ds_read_b128 v[124:127], v174 offset:12288
	ds_read_b128 v[224:227], v174 offset:18432
	v_exp_f32_e32 v72, v72
	v_exp_f32_e32 v73, v73
	v_exp_f32_e32 v74, v74
	v_exp_f32_e32 v75, v75
	v_exp_f32_e32 v76, v76
	v_exp_f32_e32 v77, v77
	s_waitcnt lgkmcnt(5)
	v_mfma_f32_32x32x16_bf16 v[98:113], v[208:211], v[138:141], v[98:113]
	v_add_u32_e32 v174, s98, v205
	v_exp_f32_e32 v78, v78
	v_exp_f32_e32 v79, v79
	ds_read_b128 v[228:231], v174 offset:12288
	ds_read_b128 v[232:235], v174 offset:18432
	v_exp_f32_e32 v80, v80
	v_exp_f32_e32 v81, v81
	v_add_u32_e32 v174, s98, v206
	s_waitcnt lgkmcnt(6)
	v_mfma_f32_32x32x16_bf16 v[82:97], v[212:215], v[138:141], v[82:97]
	v_add_f32_e64 v212, v50, v66
	v_add_f32_e64 v213, v51, v67
	v_add_f32_e64 v214, v52, v68
	v_add_f32_e64 v215, v53, v69
	v_lshl_add_u32 v202, s89, 14, v115
	v_add_f32_e32 v212, v214, v212
	v_add_f32_e32 v213, v215, v213
	v_add_f32_e32 v214, v54, v70
	v_add_f32_e32 v215, v55, v71
	ds_read_b128 v[208:211], v174 offset:12288
	ds_read_b128 v[236:239], v174 offset:18432
	v_add_f32_e32 v212, v214, v212
	v_add_f32_e32 v213, v215, v213
	s_waitcnt lgkmcnt(4)
	v_mfma_f32_32x32x16_bf16 v[98:113], v[216:219], v[134:137], v[98:113]
	v_add_f32_e64 v214, v56, v72
	v_add_f32_e64 v215, v57, v73
	v_cvt_pk_bf16_f32 v50, v50, v51
	v_cvt_pk_bf16_f32 v51, v52, v53
	v_cvt_pk_bf16_f32 v52, v54, v55
	v_cvt_pk_bf16_f32 v53, v56, v57
	v_cvt_pk_bf16_f32 v54, v58, v59
	v_add_f32_e64 v212, v214, v212
	v_add_f32_e64 v213, v215, v213
	v_mfma_f32_32x32x16_bf16 v[82:97], v[220:223], v[134:137], v[82:97]
	v_add_f32_e64 v214, v58, v74
	v_add_f32_e64 v215, v59, v75
	v_cvt_pk_bf16_f32 v55, v60, v61
	v_cvt_pk_bf16_f32 v56, v62, v63
	v_cvt_pk_bf16_f32 v57, v64, v65
	v_cvt_pk_bf16_f32 v58, v66, v67
	v_cvt_pk_bf16_f32 v59, v68, v69
	v_add_f32_e64 v212, v214, v212
	v_add_f32_e64 v213, v215, v213
	v_mfma_f32_32x32x16_bf16 v[98:113], v[124:127], v[130:133], v[98:113]
	v_add_f32_e64 v214, v60, v76
	v_add_f32_e64 v215, v61, v77
	v_add_f32_e64 v126, v62, v78
	v_add_f32_e64 v127, v63, v79
	v_add_f32_e64 v124, v214, v212
	v_add_f32_e64 v125, v215, v213
	v_cvt_pk_bf16_f32 v60, v70, v71
	v_cvt_pk_bf16_f32 v61, v72, v73
	v_cvt_pk_bf16_f32 v62, v74, v75
	v_cvt_pk_bf16_f32 v63, v76, v77
	v_mfma_f32_32x32x16_bf16 v[82:97], v[224:227], v[130:133], v[82:97]
	v_add_f32_e64 v124, v126, v124
	v_add_f32_e64 v125, v127, v125
	v_add_f32_e64 v126, v64, v80
	v_add_f32_e64 v127, v65, v81
	v_cvt_pk_bf16_f32 v64, v78, v79
	v_cvt_pk_bf16_f32 v65, v80, v81
	ds_read_b64_tr_b16 v[66:67], v202 offset:0
	ds_read_b64_tr_b16 v[68:69], v202 offset:0x400
	ds_read_b64_tr_b16 v[70:71], v202 offset:0x800
	s_waitcnt lgkmcnt(6)
	v_mfma_f32_32x32x16_bf16 v[98:113], v[228:231], v[146:149], v[98:113]
	ds_read_b64_tr_b16 v[72:73], v202 offset:0xc00
	ds_read_b64_tr_b16 v[74:75], v202 offset:0x1000
	ds_read_b64_tr_b16 v[76:77], v202 offset:0x1400
	ds_read_b64_tr_b16 v[78:79], v202 offset:0x1800
	ds_read_b64_tr_b16 v[80:81], v202 offset:0x1c00
	v_add_f32_e64 v124, v126, v124
	v_add_f32_e64 v125, v127, v125
	s_waitcnt lgkmcnt(9)
	v_mfma_f32_32x32x16_bf16 v[82:97], v[232:235], v[146:149], v[82:97]
	v_add_f32_e32 v124, v124, v125

; DEVI void finishSM(f32x16& p0, f32x16& p1, float alpha, float& l_reg, bf16x8& pa0, bf16x8& pa1, bf16x8& pa2, bf16x8& pa3) {
;     ...
;     { auto rr = __builtin_amdgcn_permlane32_swap(__float_as_uint(ps), __float_as_uint(ps), false, false);
;       ps = __uint_as_float(rr[0]) + __uint_as_float(rr[1]); }
	v_mov_b32_e32 v125, v124


; template <int OFF> DEVI s16x4 tr_read(int vb) { s16x4 r; asm volatile("ds_read_b64_tr_b16 %0, %1 offset:%2" : "=&v"(r) : "v"(vb), "i"(OFF) : "memory"); return r; }
; DEVI void pv_both(f32x16& o0, f32x16& o1, int vb, bf16x8 pa0, bf16x8 pa1, bf16x8 pa2, bf16x8 pa3) {
;     const s16x4 a0 = tr_read<v_rd_off(0, 0, 0)>(vb), b0 = tr_read<v_rd_off(0, 0, 1)>(vb), a1 = tr_read<v_rd_off(0, 1, 0)>(vb), b1 = tr_read<v_rd_off(0, 1, 1)>(vb);
;     const s16x4 a2 = tr_read<v_rd_off(0, 2, 0)>(vb), b2 = tr_read<v_rd_off(0, 2, 1)>(vb), a3 = tr_read<v_rd_off(0, 3, 0)>(vb), b3 = tr_read<v_rd_off(0, 3, 1)>(vb);
;     const s16x4 c0 = tr_read<v_rd_off(1, 0, 0)>(vb), d0 = tr_read<v_rd_off(1, 0, 1)>(vb), c1 = tr_read<v_rd_off(1, 1, 0)>(vb), d1 = tr_read<v_rd_off(1, 1, 1)>(vb);
;     const s16x4 c2 = tr_read<v_rd_off(1, 2, 0)>(vb), d2 = tr_read<v_rd_off(1, 2, 1)>(vb), c3 = tr_read<v_rd_off(1, 3, 0)>(vb), d3 = tr_read<v_rd_off(1, 3, 1)>(vb);
;     asm volatile("s_waitcnt lgkmcnt(8)" ::: "memory"); SBAR();
;     ...
;     o0 = __builtin_amdgcn_mfma_f32_32x32x16_bf16(pa0, PK(a0, b0), o0, 0, 0, 0);
;     o0 = __builtin_amdgcn_mfma_f32_32x32x16_bf16(pa1, PK(a1, b1), o0, 0, 0, 0);
;     o0 = __builtin_amdgcn_mfma_f32_32x32x16_bf16(pa2, PK(a2, b2), o0, 0, 0, 0);
;     o0 = __builtin_amdgcn_mfma_f32_32x32x16_bf16(pa3, PK(a3, b3), o0, 0, 0, 0);
;     asm volatile("s_waitcnt lgkmcnt(0)" ::: "memory"); SBAR();
;     o1 = __builtin_amdgcn_mfma_f32_32x32x16_bf16(pa0, PK(c0, d0), o1, 0, 0, 0);
;     o1 = __builtin_amdgcn_mfma_f32_32x32x16_bf16(pa1, PK(c1, d1), o1, 0, 0, 0);
;     o1 = __builtin_amdgcn_mfma_f32_32x32x16_bf16(pa2, PK(c2, d2), o1, 0, 0, 0);
;     o1 = __builtin_amdgcn_mfma_f32_32x32x16_bf16(pa3, PK(c3, d3), o1, 0, 0, 0);
;     ...
; }
; template <bool FIRST> DEVI bool partialSM(f32x16& p0, f32x16& p1, float& m_reg, float& alpha) {
;     float pmax = p0[0];
; #pragma unroll
;     for (int r = 1; r < 16; ++r) pmax = fmaxf(pmax, p0[r]);
; #pragma unroll
;     for (int r = 0; r < 16; ++r) pmax = fmaxf(pmax, p1[r]);
;     { auto rr = __builtin_amdgcn_permlane32_swap(__float_as_uint(pmax), __float_as_uint(pmax), false, false);
;       pmax = fmaxf(__uint_as_float(rr[0]), __uint_as_float(rr[1])); }
;     if (FIRST) { m_reg = pmax; alpha = 1.f;
; #pragma unroll
;         for (int r = 0; r < 16; ++r) { p0[r] = __builtin_amdgcn_exp2f(p0[r] - pmax); p1[r] = p1[r] - pmax; }
	v_mfma_f32_32x32x16_bf16 v[98:113], v[208:211], v[142:145], v[98:113]
	v_permlane32_swap_b32_e32 v124, v125
	ds_read_b64_tr_b16 v[208:209], v202 offset:0x200
	ds_read_b64_tr_b16 v[210:211], v202 offset:0x600
	ds_read_b64_tr_b16 v[212:213], v202 offset:0xa00
	ds_read_b64_tr_b16 v[214:215], v202 offset:0xe00
	ds_read_b64_tr_b16 v[216:217], v202 offset:0x1200
	ds_read_b64_tr_b16 v[218:219], v202 offset:0x1600
	ds_read_b64_tr_b16 v[220:221], v202 offset:0x1a00
	s_waitcnt lgkmcnt(15)
	v_mfma_f32_32x32x16_bf16 v[82:97], v[236:239], v[142:145], v[82:97]
	ds_read_b64_tr_b16 v[222:223], v202 offset:0x1e00
	s_waitcnt lgkmcnt(4)
	v_mfma_f32_32x32x16_bf16 v[18:33], v[50:53], v[66:69], v[18:33]
	v_mfma_f32_32x32x16_bf16 v[2:17], v[50:53], v[208:211], v[2:17]
	s_nop 1
	v_max_f32_e32 v249, v99, v99
	v_max_f32_e32 v250, v98, v98
	v_max_f32_e32 v249, v250, v249
	v_max3_f32 v249, v249, v100, v101
	v_max3_f32 v249, v249, v102, v103
	v_max3_f32 v251, v249, v104, v105
	v_max3_f32 v251, v251, v106, v107
	v_exp_f32_e32 v50, v98
	v_exp_f32_e32 v51, v99
	v_exp_f32_e32 v52, v100
	v_exp_f32_e32 v53, v101
	v_mfma_f32_32x32x16_bf16 v[18:33], v[54:57], v[70:73], v[18:33]
	v_mfma_f32_32x32x16_bf16 v[2:17], v[54:57], v[212:215], v[2:17]
	v_max3_f32 v251, v251, v108, v109
	v_max3_f32 v251, v251, v110, v111
	v_max3_f32 v251, v251, v112, v113
	v_max3_f32 v251, v251, v82, v83
	v_max3_f32 v251, v251, v84, v85
	v_max3_f32 v251, v251, v86, v87
	v_max3_f32 v251, v251, v88, v89
	v_exp_f32_e32 v54, v102
	v_exp_f32_e32 v55, v103
	v_exp_f32_e32 v56, v104
	v_exp_f32_e32 v57, v105
	v_mfma_f32_32x32x16_bf16 v[18:33], v[58:61], v[74:77], v[18:33]
	s_waitcnt lgkmcnt(0)
	v_mfma_f32_32x32x16_bf16 v[2:17], v[58:61], v[216:219], v[2:17]
	v_max3_f32 v251, v251, v90, v91
	v_max3_f32 v251, v251, v92, v93
	v_max3_f32 v251, v251, v94, v95
	v_max3_f32 v251, v251, v96, v97
	v_mov_b32_e32 v252, v251


; DEVI void pv_both(f32x16& o0, f32x16& o1, int vb, bf16x8 pa0, bf16x8 pa1, bf16x8 pa2, bf16x8 pa3) {
;     ...
;     o1 = __builtin_amdgcn_mfma_f32_32x32x16_bf16(pa1, PK(c1, d1), o1, 0, 0, 0);
;     o1 = __builtin_amdgcn_mfma_f32_32x32x16_bf16(pa2, PK(c2, d2), o1, 0, 0, 0);
;     o1 = __builtin_amdgcn_mfma_f32_32x32x16_bf16(pa3, PK(c3, d3), o1, 0, 0, 0);
;     ...
; }
; template <bool FIRST> DEVI bool partialSM(f32x16& p0, f32x16& p1, float& m_reg, float& alpha) {
;     float pmax = p0[0];
; #pragma unroll
;     for (int r = 1; r < 16; ++r) pmax = fmaxf(pmax, p0[r]);
; #pragma unroll
;     for (int r = 0; r < 16; ++r) pmax = fmaxf(pmax, p1[r]);
;     { auto rr = __builtin_amdgcn_permlane32_swap(__float_as_uint(pmax), __float_as_uint(pmax), false, false);
;       pmax = fmaxf(__uint_as_float(rr[0]), __uint_as_float(rr[1])); }
;     if (FIRST) { m_reg = pmax; alpha = 1.f;
; #pragma unroll
;         for (int r = 0; r < 16; ++r) { p0[r] = __builtin_amdgcn_exp2f(p0[r] - pmax); p1[r] = p1[r] - pmax; }
;         return false;
;     } else if (__builtin_expect(__all(pmax <= ATT_THR), 1)) { alpha = 1.f;
; #pragma unroll
;         for (int r = 0; r < 16; ++r) p0[r] = __builtin_amdgcn_exp2f(p0[r]);
;         return false;
;     } else { const float d = fmaxf(pmax, 0.f); alpha = __builtin_amdgcn_exp2f(-d); m_reg += d;
	v_exp_f32_e32 v58, v106
	v_exp_f32_e32 v59, v107
	v_permlane32_swap_b32_e32 v251, v252
	v_exp_f32_e32 v60, v108
	v_exp_f32_e32 v61, v109
	v_mfma_f32_32x32x16_bf16 v[18:33], v[62:65], v[78:81], v[18:33]
	v_mfma_f32_32x32x16_bf16 v[2:17], v[62:65], v[220:223], v[2:17]
	v_exp_f32_e32 v62, v110
	v_exp_f32_e32 v63, v111
	v_exp_f32_e32 v64, v112
	v_exp_f32_e32 v65, v113
	v_max_f32_e32 v252, v252, v252
	v_max_f32_e32 v251, v251, v251
	v_max_f32_e32 v126, v251, v252
	v_cmp_ge_f32_e32 vcc, s79, v126
	s_cmp_lg_u64 vcc, exec
	s_cselect_b64 s[6:7], -1, 0
	s_cbranch_scc1 .LBB0_705
	v_mov_b32_e32 v208, 1.0

; DEVI void finishSM(f32x16& p0, f32x16& p1, float alpha, float& l_reg, bf16x8& pa0, bf16x8& pa1, bf16x8& pa2, bf16x8& pa3) {
; #pragma unroll
;     for (int r = 0; r < 16; ++r) p1[r] = __builtin_amdgcn_exp2f(p1[r]);
	v_exp_f32_e32 v82, v82
	v_exp_f32_e32 v83, v83
	v_exp_f32_e32 v84, v84
	v_exp_f32_e32 v85, v85
	v_exp_f32_e32 v86, v86
	v_exp_f32_e32 v87, v87
	v_exp_f32_e32 v88, v88
	v_exp_f32_e32 v89, v89
	v_exp_f32_e32 v90, v90
	v_exp_f32_e32 v91, v91
	v_exp_f32_e32 v92, v92
	v_exp_f32_e32 v93, v93
	v_exp_f32_e32 v94, v94
	v_exp_f32_e32 v95, v95
	v_exp_f32_e32 v96, v96
	v_exp_f32_e32 v97, v97
	s_branch .LBB0_699

; DEVI void attn_unit8(const Params& p, char* smem, int unit, int l, int& cvs  , CvRun& crun) {
;     ...
;         const char* Kb = K_lds + s0 * 24576; const int vb = vb0 + s0 * 16384;
;         CvRegs cvr; cv_issue(p, l, cvs, lane, cvr, crun); cvs += (int)gridDim.x * 8;
;         qkt(pB0, pB1, Kb + 12288, qr, r32, hi, cinit);
.LBB0_702:
	s_mul_i32 s98, s2, 0x6000
	s_add_i32 s98, s96, s98
	s_lshl_b32 s99, s2, 14
	s_add_i32 s99, s97, s99
	s_mul_i32 s6, s61, 0x6000
	s_add_i32 s6, s6, 0
	v_add_u32_e32 v249, s6, v129

; DEVI void qkt(f32x16& p0, f32x16& p1, const char* Kb, const bf16x8 (&qr)[6], int r32, int hi, const f32x16& cinit) {
; #pragma unroll
;     for (int d0 = 0; d0 < 6; ++d0) { const int cb = (d0 * 16 + hi * 8) * 2;
;         const bf16x8 k0 = *(const bf16x8*)(Kb + KSWZ(r32, cb)), k1 = *(const bf16x8*)(Kb + KSWZ(32 + r32, cb));
;         p0 = __builtin_amdgcn_mfma_f32_32x32x16_bf16(k0, qr[d0], d0 == 0 ? cinit : p0, 0, 0, 0);
;         p1 = __builtin_amdgcn_mfma_f32_32x32x16_bf16(k1, qr[d0], d0 == 0 ? cinit : p1, 0, 0, 0); }
	s_mov_b32 m0, s98
	s_barrier
	ds_read_b128 v[234:237], v249
	ds_read_b128 v[210:213], v249 offset:6144
	global_load_lds_dwordx4 v118, s[12:13]
	s_waitcnt lgkmcnt(0)
	v_mfma_f32_32x32x16_bf16 v[98:113], v[234:237], v[150:153], v[34:49]
	s_add_i32 m0, s98, 0x2000

; DEVI void qkt(f32x16& p0, f32x16& p1, const char* Kb, const bf16x8 (&qr)[6], int r32, int hi, const f32x16& cinit) {
; #pragma unroll
;     for (int d0 = 0; d0 < 6; ++d0) { const int cb = (d0 * 16 + hi * 8) * 2;
;         const bf16x8 k0 = *(const bf16x8*)(Kb + KSWZ(r32, cb)), k1 = *(const bf16x8*)(Kb + KSWZ(32 + r32, cb));
;         p0 = __builtin_amdgcn_mfma_f32_32x32x16_bf16(k0, qr[d0], d0 == 0 ? cinit : p0, 0, 0, 0);
;         p1 = __builtin_amdgcn_mfma_f32_32x32x16_bf16(k1, qr[d0], d0 == 0 ? cinit : p1, 0, 0, 0); }
	v_add_u32_e32 v126, s6, v184
	global_load_lds_dwordx4 v120, s[12:13]
	v_mfma_f32_32x32x16_bf16 v[66:81], v[210:213], v[150:153], v[34:49]
	ds_read_b128 v[210:213], v126
	ds_read_b128 v[214:217], v126 offset:6144
	s_add_i32 m0, s98, 0x4000

; DEVI void qkt(f32x16& p0, f32x16& p1, const char* Kb, const bf16x8 (&qr)[6], int r32, int hi, const f32x16& cinit) {
; #pragma unroll
;     for (int d0 = 0; d0 < 6; ++d0) { const int cb = (d0 * 16 + hi * 8) * 2;
;         const bf16x8 k0 = *(const bf16x8*)(Kb + KSWZ(r32, cb)), k1 = *(const bf16x8*)(Kb + KSWZ(32 + r32, cb));
;         p0 = __builtin_amdgcn_mfma_f32_32x32x16_bf16(k0, qr[d0], d0 == 0 ? cinit : p0, 0, 0, 0);
;         p1 = __builtin_amdgcn_mfma_f32_32x32x16_bf16(k1, qr[d0], d0 == 0 ? cinit : p1, 0, 0, 0); }
	v_add_u32_e32 v126, s6, v185
	global_load_lds_dwordx4 v122, s[12:13]
	s_mov_b32 m0, s99
	s_waitcnt lgkmcnt(0)
	v_mfma_f32_32x32x16_bf16 v[98:113], v[210:213], v[138:141], v[98:113]


	global_load_lds_dwordx4 v116, s[44:45]
	s_add_i32 m0, s99, 0x2000


; template <int OFF> DEVI s16x4 tr_read(int vb) { s16x4 r; asm volatile("ds_read_b64_tr_b16 %0, %1 offset:%2" : "=&v"(r) : "v"(vb), "i"(OFF) : "memory"); return r; }
; DEVI void pv_both(f32x16& o0, f32x16& o1, int vb, bf16x8 pa0, bf16x8 pa1, bf16x8 pa2, bf16x8 pa3) {
;     const s16x4 a0 = tr_read<v_rd_off(0, 0, 0)>(vb), b0 = tr_read<v_rd_off(0, 0, 1)>(vb), a1 = tr_read<v_rd_off(0, 1, 0)>(vb), b1 = tr_read<v_rd_off(0, 1, 1)>(vb);
;     const s16x4 a2 = tr_read<v_rd_off(0, 2, 0)>(vb), b2 = tr_read<v_rd_off(0, 2, 1)>(vb), a3 = tr_read<v_rd_off(0, 3, 0)>(vb), b3 = tr_read<v_rd_off(0, 3, 1)>(vb);
;     const s16x4 c0 = tr_read<v_rd_off(1, 0, 0)>(vb), d0 = tr_read<v_rd_off(1, 0, 1)>(vb), c1 = tr_read<v_rd_off(1, 1, 0)>(vb), d1 = tr_read<v_rd_off(1, 1, 1)>(vb);
;     const s16x4 c2 = tr_read<v_rd_off(1, 2, 0)>(vb), d2 = tr_read<v_rd_off(1, 2, 1)>(vb), c3 = tr_read<v_rd_off(1, 3, 0)>(vb), d3 = tr_read<v_rd_off(1, 3, 1)>(vb);
; DEVI void finishSM(f32x16& p0, f32x16& p1, float alpha, float& l_reg, bf16x8& pa0, bf16x8& pa1, bf16x8& pa2, bf16x8& pa3) {
; #pragma unroll
;     for (int r = 0; r < 16; ++r) p1[r] = __builtin_amdgcn_exp2f(p1[r]);
;     f32x2 s2 = (f32x2){p0[0], p0[1]} + (f32x2){p1[0], p1[1]};
; #pragma unroll
;     for (int r = 2; r < 16; r += 2) s2 += (f32x2){p0[r], p0[r + 1]} + (f32x2){p1[r], p1[r + 1]};
;     float ps = s2[0] + s2[1];
;     { auto rr = __builtin_amdgcn_permlane32_swap(__float_as_uint(ps), __float_as_uint(ps), false, false);
;       ps = __uint_as_float(rr[0]) + __uint_as_float(rr[1]); }
;     l_reg = l_reg * alpha + ps;
;     ...
;     PK4(p0, 0, pa0); PK4(p0, 8, pa1); PK4(p1, 0, pa2); PK4(p1, 8, pa3);
;     ...
; }
; DEVI void qkt(f32x16& p0, f32x16& p1, const char* Kb, const bf16x8 (&qr)[6], int r32, int hi, const f32x16& cinit) {
; #pragma unroll
;     for (int d0 = 0; d0 < 6; ++d0) { const int cb = (d0 * 16 + hi * 8) * 2;
;         const bf16x8 k0 = *(const bf16x8*)(Kb + KSWZ(r32, cb)), k1 = *(const bf16x8*)(Kb + KSWZ(32 + r32, cb));
;         p0 = __builtin_amdgcn_mfma_f32_32x32x16_bf16(k0, qr[d0], d0 == 0 ? cinit : p0, 0, 0, 0);
;         p1 = __builtin_amdgcn_mfma_f32_32x32x16_bf16(k1, qr[d0], d0 == 0 ? cinit : p1, 0, 0, 0); }
	v_mfma_f32_32x32x16_bf16 v[66:81], v[214:217], v[138:141], v[66:81]
	global_load_lds_dwordx4 v117, s[44:45]
	ds_read_b128 v[210:213], v126
	ds_read_b128 v[214:217], v126 offset:6144
	v_add_u32_e32 v126, s6, v204
	s_waitcnt lgkmcnt(1)
	v_mfma_f32_32x32x16_bf16 v[98:113], v[210:213], v[134:137], v[98:113]
	ds_read_b128 v[210:213], v126
	ds_read_b128 v[218:221], v126 offset:6144
	v_add_u32_e32 v126, s6, v205
	s_waitcnt lgkmcnt(2)
	v_mfma_f32_32x32x16_bf16 v[66:81], v[214:217], v[134:137], v[66:81]
	ds_read_b128 v[214:217], v126
	ds_read_b128 v[222:225], v126 offset:6144
	v_add_u32_e32 v126, s6, v206
	ds_read_b128 v[226:229], v126
	ds_read_b128 v[230:233], v126 offset:6144
	v_add_f32_e32 v126, v50, v82
	v_add_f32_e32 v127, v51, v83
	v_cvt_pk_bf16_f32 v50, v50, v51
	v_cvt_pk_bf16_f32 v51, v52, v53
	s_waitcnt lgkmcnt(2)
	v_mfma_f32_32x32x16_bf16 v[98:113], v[210:213], v[130:133], v[98:113]
	v_add_f32_e64 v210, v52, v84
	v_add_f32_e64 v211, v53, v85
	v_cvt_pk_bf16_f32 v52, v54, v55
	v_cvt_pk_bf16_f32 v53, v56, v57
	v_add_f32_e64 v126, v210, v126
	v_add_f32_e64 v127, v211, v127
	v_add_f32_e64 v210, v54, v86
	v_add_f32_e64 v211, v55, v87
	v_cvt_pk_bf16_f32 v54, v58, v59
	v_mfma_f32_32x32x16_bf16 v[66:81], v[218:221], v[130:133], v[66:81]
	v_add_f32_e64 v126, v210, v126
	v_add_f32_e64 v127, v211, v127
	v_add_f32_e64 v210, v56, v88
	v_add_f32_e64 v211, v57, v89
	v_cvt_pk_bf16_f32 v55, v60, v61
	v_cvt_pk_bf16_f32 v56, v62, v63
	v_cvt_pk_bf16_f32 v57, v64, v65
	v_add_f32_e64 v126, v210, v126
	v_add_f32_e64 v127, v211, v127
	v_add_f32_e32 v210, v58, v90
	v_add_f32_e32 v211, v59, v91
	v_cvt_pk_bf16_f32 v58, v82, v83
	v_cvt_pk_bf16_f32 v59, v84, v85
	v_mfma_f32_32x32x16_bf16 v[98:113], v[214:217], v[146:149], v[98:113]
	v_add_f32_e64 v126, v210, v126
	v_add_f32_e64 v127, v211, v127
	v_add_f32_e64 v210, v60, v92
	v_add_f32_e64 v211, v61, v93
	v_cvt_pk_bf16_f32 v60, v86, v87
	v_cvt_pk_bf16_f32 v61, v88, v89
	v_add_f32_e64 v126, v210, v126
	v_add_f32_e64 v127, v211, v127
	v_add_f32_e32 v210, v62, v94
	v_add_f32_e32 v211, v63, v95
	v_cvt_pk_bf16_f32 v62, v90, v91
	v_cvt_pk_bf16_f32 v63, v92, v93
	v_mfma_f32_32x32x16_bf16 v[66:81], v[222:225], v[146:149], v[66:81]
	v_add_f32_e64 v126, v210, v126
	v_add_f32_e64 v127, v211, v127
	v_add_f32_e64 v210, v64, v96
	v_add_f32_e64 v211, v65, v97
	v_cvt_pk_bf16_f32 v64, v94, v95
	v_cvt_pk_bf16_f32 v65, v96, v97
	ds_read_b64_tr_b16 v[154:155], v202 offset:0x2000
	ds_read_b64_tr_b16 v[156:157], v202 offset:0x2400
	ds_read_b64_tr_b16 v[158:159], v202 offset:0x2800
	ds_read_b64_tr_b16 v[160:161], v202 offset:0x2c00
	ds_read_b64_tr_b16 v[162:163], v202 offset:0x3000
	ds_read_b64_tr_b16 v[164:165], v202 offset:0x3400
	ds_read_b64_tr_b16 v[166:167], v202 offset:0x3800
	ds_read_b64_tr_b16 v[168:169], v202 offset:0x3c00
	v_add_f32_e64 v126, v210, v126
	v_add_f32_e64 v127, v211, v127
	ds_read_b64_tr_b16 v[210:211], v202 offset:0x2200
	ds_read_b64_tr_b16 v[212:213], v202 offset:0x2600
	ds_read_b64_tr_b16 v[214:215], v202 offset:0x2a00
	s_waitcnt lgkmcnt(12)
	v_mfma_f32_32x32x16_bf16 v[98:113], v[226:229], v[142:145], v[98:113]
	ds_read_b64_tr_b16 v[216:217], v202 offset:0x2e00
	ds_read_b64_tr_b16 v[218:219], v202 offset:0x3200
	ds_read_b64_tr_b16 v[220:221], v202 offset:0x3600
	ds_read_b64_tr_b16 v[222:223], v202 offset:0x3a00
	ds_read_b64_tr_b16 v[224:225], v202 offset:0x3e00
	v_add_f32_e32 v126, v126, v127
	s_waitcnt lgkmcnt(6)
	v_mfma_f32_32x32x16_bf16 v[66:81], v[230:233], v[142:145], v[66:81]
	v_mov_b32_e32 v127, v126


; #define SBAR() __builtin_amdgcn_sched_barrier(0)
; DEVI void pv_both(f32x16& o0, f32x16& o1, int vb, bf16x8 pa0, bf16x8 pa1, bf16x8 pa2, bf16x8 pa3) {
;     ...
;     o0 = __builtin_amdgcn_mfma_f32_32x32x16_bf16(pa0, PK(a0, b0), o0, 0, 0, 0);
;     o0 = __builtin_amdgcn_mfma_f32_32x32x16_bf16(pa1, PK(a1, b1), o0, 0, 0, 0);
;     o0 = __builtin_amdgcn_mfma_f32_32x32x16_bf16(pa2, PK(a2, b2), o0, 0, 0, 0);
;     o0 = __builtin_amdgcn_mfma_f32_32x32x16_bf16(pa3, PK(a3, b3), o0, 0, 0, 0);
;     asm volatile("s_waitcnt lgkmcnt(0)" ::: "memory"); SBAR();
;     o1 = __builtin_amdgcn_mfma_f32_32x32x16_bf16(pa0, PK(c0, d0), o1, 0, 0, 0);
;     o1 = __builtin_amdgcn_mfma_f32_32x32x16_bf16(pa1, PK(c1, d1), o1, 0, 0, 0);
;     o1 = __builtin_amdgcn_mfma_f32_32x32x16_bf16(pa2, PK(c2, d2), o1, 0, 0, 0);
;     o1 = __builtin_amdgcn_mfma_f32_32x32x16_bf16(pa3, PK(c3, d3), o1, 0, 0, 0);
;     ...
; }
; template <bool FIRST> DEVI bool partialSM(f32x16& p0, f32x16& p1, float& m_reg, float& alpha) {
;     float pmax = p0[0];
; #pragma unroll
;     for (int r = 1; r < 16; ++r) pmax = fmaxf(pmax, p0[r]);
; #pragma unroll
;     for (int r = 0; r < 16; ++r) pmax = fmaxf(pmax, p1[r]);
;     { auto rr = __builtin_amdgcn_permlane32_swap(__float_as_uint(pmax), __float_as_uint(pmax), false, false);
;       pmax = fmaxf(__uint_as_float(rr[0]), __uint_as_float(rr[1])); }
;     if (FIRST) { m_reg = pmax; alpha = 1.f;
; #pragma unroll
;         for (int r = 0; r < 16; ++r) { p0[r] = __builtin_amdgcn_exp2f(p0[r] - pmax); p1[r] = p1[r] - pmax; }
;         return false;
;     } else if (__builtin_expect(__all(pmax <= ATT_THR), 1)) { alpha = 1.f;
; #pragma unroll
;         for (int r = 0; r < 16; ++r) p0[r] = __builtin_amdgcn_exp2f(p0[r]);
	v_mfma_f32_32x32x16_bf16 v[18:33], v[50:53], v[154:157], v[18:33]
	v_permlane32_swap_b32_e32 v126, v127
	v_mfma_f32_32x32x16_bf16 v[2:17], v[50:53], v[210:213], v[2:17]
	s_nop 1
	v_max_f32_e32 v249, v99, v99
	v_max_f32_e32 v250, v98, v98
	v_max_f32_e32 v249, v250, v249
	v_max3_f32 v249, v249, v100, v101
	v_max3_f32 v249, v249, v102, v103
	v_max3_f32 v251, v249, v104, v105
	v_max3_f32 v251, v251, v106, v107
	v_exp_f32_e32 v50, v98
	v_exp_f32_e32 v51, v99
	v_exp_f32_e32 v52, v100
	v_exp_f32_e32 v53, v101
	v_mfma_f32_32x32x16_bf16 v[18:33], v[54:57], v[158:161], v[18:33]
	s_waitcnt lgkmcnt(2)
	v_mfma_f32_32x32x16_bf16 v[2:17], v[54:57], v[214:217], v[2:17]
	v_max3_f32 v251, v251, v108, v109
	v_max3_f32 v251, v251, v110, v111
	v_max3_f32 v251, v251, v112, v113
	v_max3_f32 v251, v251, v66, v67
	v_max3_f32 v251, v251, v68, v69
	v_max3_f32 v251, v251, v70, v71
	v_max3_f32 v251, v251, v72, v73
	v_exp_f32_e32 v54, v102
	v_exp_f32_e32 v55, v103
	v_exp_f32_e32 v56, v104
	v_exp_f32_e32 v57, v105
	v_mfma_f32_32x32x16_bf16 v[18:33], v[58:61], v[162:165], v[18:33]
	v_mfma_f32_32x32x16_bf16 v[2:17], v[58:61], v[218:221], v[2:17]
	v_max3_f32 v251, v251, v74, v75
	v_max3_f32 v251, v251, v76, v77
	v_max3_f32 v251, v251, v78, v79
	v_max3_f32 v251, v251, v80, v81
	v_mov_b32_e32 v252, v251


; DEVI void pv_both(f32x16& o0, f32x16& o1, int vb, bf16x8 pa0, bf16x8 pa1, bf16x8 pa2, bf16x8 pa3) {
;     ...
;     o1 = __builtin_amdgcn_mfma_f32_32x32x16_bf16(pa1, PK(c1, d1), o1, 0, 0, 0);
;     o1 = __builtin_amdgcn_mfma_f32_32x32x16_bf16(pa2, PK(c2, d2), o1, 0, 0, 0);
;     o1 = __builtin_amdgcn_mfma_f32_32x32x16_bf16(pa3, PK(c3, d3), o1, 0, 0, 0);
;     ...
; }
; template <bool FIRST> DEVI bool partialSM(f32x16& p0, f32x16& p1, float& m_reg, float& alpha) {
;     float pmax = p0[0];
; #pragma unroll
;     for (int r = 1; r < 16; ++r) pmax = fmaxf(pmax, p0[r]);
; #pragma unroll
;     for (int r = 0; r < 16; ++r) pmax = fmaxf(pmax, p1[r]);
;     { auto rr = __builtin_amdgcn_permlane32_swap(__float_as_uint(pmax), __float_as_uint(pmax), false, false);
;       pmax = fmaxf(__uint_as_float(rr[0]), __uint_as_float(rr[1])); }
;     if (FIRST) { m_reg = pmax; alpha = 1.f;
; #pragma unroll
;         for (int r = 0; r < 16; ++r) { p0[r] = __builtin_amdgcn_exp2f(p0[r] - pmax); p1[r] = p1[r] - pmax; }
;         return false;
;     } else if (__builtin_expect(__all(pmax <= ATT_THR), 1)) { alpha = 1.f;
; #pragma unroll
;         for (int r = 0; r < 16; ++r) p0[r] = __builtin_amdgcn_exp2f(p0[r]);
;         return false;
;     } else { const float d = fmaxf(pmax, 0.f); alpha = __builtin_amdgcn_exp2f(-d); m_reg += d;
	v_exp_f32_e32 v58, v106
	v_exp_f32_e32 v59, v107
	v_permlane32_swap_b32_e32 v251, v252
	v_exp_f32_e32 v60, v108
	v_exp_f32_e32 v61, v109
	v_mfma_f32_32x32x16_bf16 v[18:33], v[62:65], v[166:169], v[18:33]
	s_waitcnt lgkmcnt(0)
	v_mfma_f32_32x32x16_bf16 v[2:17], v[62:65], v[222:225], v[2:17]
	v_exp_f32_e32 v62, v110
	v_exp_f32_e32 v63, v111
	v_exp_f32_e32 v64, v112
	v_exp_f32_e32 v65, v113
	v_max_f32_e32 v252, v252, v252
	v_max_f32_e32 v251, v251, v251
	v_max_f32_e32 v174, v251, v252
	v_cmp_ge_f32_e32 vcc, s79, v174
	s_cmp_lg_u64 vcc, exec
	s_cselect_b64 s[6:7], -1, 0
	s_cbranch_scc1 .LBB0_711
	v_mov_b32_e32 v202, 1.0

; template <bool FIRST> DEVI bool partialSM(f32x16& p0, f32x16& p1, float& m_reg, float& alpha) {
;     ...
;     } else if (__builtin_expect(__all(pmax <= ATT_THR), 1)) { alpha = 1.f;
; #pragma unroll
;         for (int r = 0; r < 16; ++r) p0[r] = __builtin_amdgcn_exp2f(p0[r]);
;         return false;
	s_branch .LBB0_716

; template <int OFF> DEVI s16x4 tr_read(int vb) { s16x4 r; asm volatile("ds_read_b64_tr_b16 %0, %1 offset:%2" : "=&v"(r) : "v"(vb), "i"(OFF) : "memory"); return r; }
; DEVI void pv_both(f32x16& o0, f32x16& o1, int vb, bf16x8 pa0, bf16x8 pa1, bf16x8 pa2, bf16x8 pa3) {
;     const s16x4 a0 = tr_read<v_rd_off(0, 0, 0)>(vb), b0 = tr_read<v_rd_off(0, 0, 1)>(vb), a1 = tr_read<v_rd_off(0, 1, 0)>(vb), b1 = tr_read<v_rd_off(0, 1, 1)>(vb);
;     const s16x4 a2 = tr_read<v_rd_off(0, 2, 0)>(vb), b2 = tr_read<v_rd_off(0, 2, 1)>(vb), a3 = tr_read<v_rd_off(0, 3, 0)>(vb), b3 = tr_read<v_rd_off(0, 3, 1)>(vb);
;     const s16x4 c0 = tr_read<v_rd_off(1, 0, 0)>(vb), d0 = tr_read<v_rd_off(1, 0, 1)>(vb), c1 = tr_read<v_rd_off(1, 1, 0)>(vb), d1 = tr_read<v_rd_off(1, 1, 1)>(vb);
;     const s16x4 c2 = tr_read<v_rd_off(1, 2, 0)>(vb), d2 = tr_read<v_rd_off(1, 2, 1)>(vb), c3 = tr_read<v_rd_off(1, 3, 0)>(vb), d3 = tr_read<v_rd_off(1, 3, 1)>(vb);
; DEVI void finishSM(f32x16& p0, f32x16& p1, float alpha, float& l_reg, bf16x8& pa0, bf16x8& pa1, bf16x8& pa2, bf16x8& pa3) {
; #pragma unroll
;     for (int r = 0; r < 16; ++r) p1[r] = __builtin_amdgcn_exp2f(p1[r]);
;     f32x2 s2 = (f32x2){p0[0], p0[1]} + (f32x2){p1[0], p1[1]};
; #pragma unroll
;     for (int r = 2; r < 16; r += 2) s2 += (f32x2){p0[r], p0[r + 1]} + (f32x2){p1[r], p1[r + 1]};
;     float ps = s2[0] + s2[1];
;     { auto rr = __builtin_amdgcn_permlane32_swap(__float_as_uint(ps), __float_as_uint(ps), false, false);
;       ps = __uint_as_float(rr[0]) + __uint_as_float(rr[1]); }
;     l_reg = l_reg * alpha + ps;
;     ...
;     PK4(p0, 0, pa0); PK4(p0, 8, pa1); PK4(p1, 0, pa2); PK4(p1, 8, pa3);
;     ...
; }
; DEVI void qkt(f32x16& p0, f32x16& p1, const char* Kb, const bf16x8 (&qr)[6], int r32, int hi, const f32x16& cinit) {
; #pragma unroll
;     for (int d0 = 0; d0 < 6; ++d0) { const int cb = (d0 * 16 + hi * 8) * 2;
;         const bf16x8 k0 = *(const bf16x8*)(Kb + KSWZ(r32, cb)), k1 = *(const bf16x8*)(Kb + KSWZ(32 + r32, cb));
;         p0 = __builtin_amdgcn_mfma_f32_32x32x16_bf16(k0, qr[d0], d0 == 0 ? cinit : p0, 0, 0, 0);
;         p1 = __builtin_amdgcn_mfma_f32_32x32x16_bf16(k1, qr[d0], d0 == 0 ? cinit : p1, 0, 0, 0); }
.LBB0_2260:
	v_add_u32_e32 v174, s98, v205
	v_exp_f32_e32 v66, v66
	v_exp_f32_e32 v67, v67
	s_waitcnt lgkmcnt(1)
	v_mfma_f32_32x32x16_bf16 v[98:113], v[82:85], v[150:153], v[34:49]
	v_add_u32_e32 v82, s98, v184
	v_add_u32_e32 v83, s98, v185
	ds_read_b128 v[210:213], v82 offset:12288
	ds_read_b128 v[214:217], v82 offset:18432
	ds_read_b128 v[218:221], v83 offset:12288
	ds_read_b128 v[222:225], v83 offset:18432
	v_exp_f32_e32 v68, v68
	v_exp_f32_e32 v69, v69
	v_exp_f32_e32 v70, v70
	v_exp_f32_e32 v71, v71
	s_waitcnt lgkmcnt(4)
	v_mfma_f32_32x32x16_bf16 v[82:97], v[124:127], v[150:153], v[34:49]
	ds_read_b128 v[124:127], v174 offset:12288
	ds_read_b128 v[226:229], v174 offset:18432
	v_exp_f32_e32 v72, v72
	v_exp_f32_e32 v73, v73
	v_exp_f32_e32 v74, v74
	v_exp_f32_e32 v75, v75
	v_exp_f32_e32 v76, v76
	v_exp_f32_e32 v77, v77
	s_waitcnt lgkmcnt(5)
	v_mfma_f32_32x32x16_bf16 v[98:113], v[210:213], v[138:141], v[98:113]
	v_add_u32_e32 v174, s98, v206
	v_exp_f32_e32 v78, v78
	v_exp_f32_e32 v79, v79
	ds_read_b128 v[230:233], v174 offset:12288
	ds_read_b128 v[234:237], v174 offset:18432
	v_exp_f32_e32 v80, v80
	v_exp_f32_e32 v81, v81
	v_add_u32_e32 v174, s98, v207
	s_waitcnt lgkmcnt(6)
	v_mfma_f32_32x32x16_bf16 v[82:97], v[214:217], v[138:141], v[82:97]
	v_add_f32_e64 v214, v50, v66
	v_add_f32_e64 v215, v51, v67
	v_add_f32_e64 v216, v52, v68
	v_add_f32_e64 v217, v53, v69
	v_lshl_add_u32 v203, s71, 14, v115
	v_add_f32_e32 v214, v216, v214
	v_add_f32_e32 v215, v217, v215
	v_add_f32_e32 v216, v54, v70
	v_add_f32_e32 v217, v55, v71
	ds_read_b128 v[210:213], v174 offset:12288
	ds_read_b128 v[238:241], v174 offset:18432
	v_add_f32_e32 v214, v216, v214
	v_add_f32_e32 v215, v217, v215
	s_waitcnt lgkmcnt(4)
	v_mfma_f32_32x32x16_bf16 v[98:113], v[218:221], v[134:137], v[98:113]
	v_add_f32_e64 v216, v56, v72
	v_add_f32_e64 v217, v57, v73
	v_cvt_pk_bf16_f32 v50, v50, v51
	v_cvt_pk_bf16_f32 v51, v52, v53
	v_cvt_pk_bf16_f32 v52, v54, v55
	v_cvt_pk_bf16_f32 v53, v56, v57
	v_cvt_pk_bf16_f32 v54, v58, v59
	v_add_f32_e64 v214, v216, v214
	v_add_f32_e64 v215, v217, v215
	v_mfma_f32_32x32x16_bf16 v[82:97], v[222:225], v[134:137], v[82:97]
	v_add_f32_e64 v216, v58, v74
	v_add_f32_e64 v217, v59, v75
	v_cvt_pk_bf16_f32 v55, v60, v61
	v_cvt_pk_bf16_f32 v56, v62, v63
	v_cvt_pk_bf16_f32 v57, v64, v65
	v_cvt_pk_bf16_f32 v58, v66, v67
	v_cvt_pk_bf16_f32 v59, v68, v69
	v_add_f32_e64 v214, v216, v214
	v_add_f32_e64 v215, v217, v215
	v_mfma_f32_32x32x16_bf16 v[98:113], v[124:127], v[130:133], v[98:113]
	v_add_f32_e64 v216, v60, v76
	v_add_f32_e64 v217, v61, v77
	v_add_f32_e64 v126, v62, v78
	v_add_f32_e64 v127, v63, v79
	v_add_f32_e64 v124, v216, v214
	v_add_f32_e64 v125, v217, v215
	v_cvt_pk_bf16_f32 v60, v70, v71
	v_cvt_pk_bf16_f32 v61, v72, v73
	v_cvt_pk_bf16_f32 v62, v74, v75
	v_cvt_pk_bf16_f32 v63, v76, v77
	v_mfma_f32_32x32x16_bf16 v[82:97], v[226:229], v[130:133], v[82:97]
	v_add_f32_e64 v124, v126, v124
	v_add_f32_e64 v125, v127, v125
	v_add_f32_e64 v126, v64, v80
	v_add_f32_e64 v127, v65, v81
	v_cvt_pk_bf16_f32 v64, v78, v79
	v_cvt_pk_bf16_f32 v65, v80, v81
	ds_read_b64_tr_b16 v[66:67], v203 offset:0
	ds_read_b64_tr_b16 v[68:69], v203 offset:0x400
	ds_read_b64_tr_b16 v[70:71], v203 offset:0x800
	s_waitcnt lgkmcnt(6)
	v_mfma_f32_32x32x16_bf16 v[98:113], v[230:233], v[146:149], v[98:113]
	ds_read_b64_tr_b16 v[72:73], v203 offset:0xc00
	ds_read_b64_tr_b16 v[74:75], v203 offset:0x1000
	ds_read_b64_tr_b16 v[76:77], v203 offset:0x1400
	ds_read_b64_tr_b16 v[78:79], v203 offset:0x1800
	ds_read_b64_tr_b16 v[80:81], v203 offset:0x1c00
	v_add_f32_e64 v124, v126, v124
	v_add_f32_e64 v125, v127, v125
	s_waitcnt lgkmcnt(9)
	v_mfma_f32_32x32x16_bf16 v[82:97], v[234:237], v[146:149], v[82:97]
	v_add_f32_e32 v124, v124, v125

; DEVI void finishSM(f32x16& p0, f32x16& p1, float alpha, float& l_reg, bf16x8& pa0, bf16x8& pa1, bf16x8& pa2, bf16x8& pa3) {
;     ...
;     { auto rr = __builtin_amdgcn_permlane32_swap(__float_as_uint(ps), __float_as_uint(ps), false, false);
;       ps = __uint_as_float(rr[0]) + __uint_as_float(rr[1]); }
	v_mov_b32_e32 v125, v124


; template <int OFF> DEVI s16x4 tr_read(int vb) { s16x4 r; asm volatile("ds_read_b64_tr_b16 %0, %1 offset:%2" : "=&v"(r) : "v"(vb), "i"(OFF) : "memory"); return r; }
; DEVI void pv_both(f32x16& o0, f32x16& o1, int vb, bf16x8 pa0, bf16x8 pa1, bf16x8 pa2, bf16x8 pa3) {
;     const s16x4 a0 = tr_read<v_rd_off(0, 0, 0)>(vb), b0 = tr_read<v_rd_off(0, 0, 1)>(vb), a1 = tr_read<v_rd_off(0, 1, 0)>(vb), b1 = tr_read<v_rd_off(0, 1, 1)>(vb);
;     const s16x4 a2 = tr_read<v_rd_off(0, 2, 0)>(vb), b2 = tr_read<v_rd_off(0, 2, 1)>(vb), a3 = tr_read<v_rd_off(0, 3, 0)>(vb), b3 = tr_read<v_rd_off(0, 3, 1)>(vb);
;     const s16x4 c0 = tr_read<v_rd_off(1, 0, 0)>(vb), d0 = tr_read<v_rd_off(1, 0, 1)>(vb), c1 = tr_read<v_rd_off(1, 1, 0)>(vb), d1 = tr_read<v_rd_off(1, 1, 1)>(vb);
;     const s16x4 c2 = tr_read<v_rd_off(1, 2, 0)>(vb), d2 = tr_read<v_rd_off(1, 2, 1)>(vb), c3 = tr_read<v_rd_off(1, 3, 0)>(vb), d3 = tr_read<v_rd_off(1, 3, 1)>(vb);
;     asm volatile("s_waitcnt lgkmcnt(8)" ::: "memory"); SBAR();
;     ...
;     o0 = __builtin_amdgcn_mfma_f32_32x32x16_bf16(pa0, PK(a0, b0), o0, 0, 0, 0);
;     o0 = __builtin_amdgcn_mfma_f32_32x32x16_bf16(pa1, PK(a1, b1), o0, 0, 0, 0);
;     o0 = __builtin_amdgcn_mfma_f32_32x32x16_bf16(pa2, PK(a2, b2), o0, 0, 0, 0);
;     o0 = __builtin_amdgcn_mfma_f32_32x32x16_bf16(pa3, PK(a3, b3), o0, 0, 0, 0);
;     asm volatile("s_waitcnt lgkmcnt(0)" ::: "memory"); SBAR();
;     o1 = __builtin_amdgcn_mfma_f32_32x32x16_bf16(pa0, PK(c0, d0), o1, 0, 0, 0);
;     o1 = __builtin_amdgcn_mfma_f32_32x32x16_bf16(pa1, PK(c1, d1), o1, 0, 0, 0);
;     o1 = __builtin_amdgcn_mfma_f32_32x32x16_bf16(pa2, PK(c2, d2), o1, 0, 0, 0);
;     o1 = __builtin_amdgcn_mfma_f32_32x32x16_bf16(pa3, PK(c3, d3), o1, 0, 0, 0);
;     ...
; }
; template <bool FIRST> DEVI bool partialSM(f32x16& p0, f32x16& p1, float& m_reg, float& alpha) {
;     float pmax = p0[0];
; #pragma unroll
;     for (int r = 1; r < 16; ++r) pmax = fmaxf(pmax, p0[r]);
; #pragma unroll
;     for (int r = 0; r < 16; ++r) pmax = fmaxf(pmax, p1[r]);
;     { auto rr = __builtin_amdgcn_permlane32_swap(__float_as_uint(pmax), __float_as_uint(pmax), false, false);
;       pmax = fmaxf(__uint_as_float(rr[0]), __uint_as_float(rr[1])); }
;     if (FIRST) { m_reg = pmax; alpha = 1.f;
; #pragma unroll
;         for (int r = 0; r < 16; ++r) { p0[r] = __builtin_amdgcn_exp2f(p0[r] - pmax); p1[r] = p1[r] - pmax; }
	v_mfma_f32_32x32x16_bf16 v[98:113], v[210:213], v[142:145], v[98:113]
	v_permlane32_swap_b32_e32 v124, v125
	ds_read_b64_tr_b16 v[210:211], v203 offset:0x200
	ds_read_b64_tr_b16 v[212:213], v203 offset:0x600
	ds_read_b64_tr_b16 v[214:215], v203 offset:0xa00
	ds_read_b64_tr_b16 v[216:217], v203 offset:0xe00
	ds_read_b64_tr_b16 v[218:219], v203 offset:0x1200
	ds_read_b64_tr_b16 v[220:221], v203 offset:0x1600
	ds_read_b64_tr_b16 v[222:223], v203 offset:0x1a00
	s_waitcnt lgkmcnt(15)
	v_mfma_f32_32x32x16_bf16 v[82:97], v[238:241], v[142:145], v[82:97]
	ds_read_b64_tr_b16 v[224:225], v203 offset:0x1e00
	s_waitcnt lgkmcnt(4)
	v_mfma_f32_32x32x16_bf16 v[18:33], v[50:53], v[66:69], v[18:33]
	v_mfma_f32_32x32x16_bf16 v[2:17], v[50:53], v[210:213], v[2:17]
	s_nop 1
	v_max_f32_e32 v249, v99, v99
	v_max_f32_e32 v250, v98, v98
	v_max_f32_e32 v249, v250, v249
	v_max3_f32 v249, v249, v100, v101
	v_max3_f32 v249, v249, v102, v103
	v_max3_f32 v251, v249, v104, v105
	v_max3_f32 v251, v251, v106, v107
	v_exp_f32_e32 v50, v98
	v_exp_f32_e32 v51, v99
	v_exp_f32_e32 v52, v100
	v_exp_f32_e32 v53, v101
	v_mfma_f32_32x32x16_bf16 v[18:33], v[54:57], v[70:73], v[18:33]
	v_mfma_f32_32x32x16_bf16 v[2:17], v[54:57], v[214:217], v[2:17]
	v_max3_f32 v251, v251, v108, v109
	v_max3_f32 v251, v251, v110, v111
	v_max3_f32 v251, v251, v112, v113
	v_max3_f32 v251, v251, v82, v83
	v_max3_f32 v251, v251, v84, v85
	v_max3_f32 v251, v251, v86, v87
	v_max3_f32 v251, v251, v88, v89
	v_exp_f32_e32 v54, v102
	v_exp_f32_e32 v55, v103
	v_exp_f32_e32 v56, v104
	v_exp_f32_e32 v57, v105
	v_mfma_f32_32x32x16_bf16 v[18:33], v[58:61], v[74:77], v[18:33]
	s_waitcnt lgkmcnt(0)
	v_mfma_f32_32x32x16_bf16 v[2:17], v[58:61], v[218:221], v[2:17]
	v_max3_f32 v251, v251, v90, v91
	v_max3_f32 v251, v251, v92, v93
	v_max3_f32 v251, v251, v94, v95
	v_max3_f32 v251, v251, v96, v97
	v_mov_b32_e32 v252, v251


; DEVI void pv_both(f32x16& o0, f32x16& o1, int vb, bf16x8 pa0, bf16x8 pa1, bf16x8 pa2, bf16x8 pa3) {
;     ...
;     o1 = __builtin_amdgcn_mfma_f32_32x32x16_bf16(pa1, PK(c1, d1), o1, 0, 0, 0);
;     o1 = __builtin_amdgcn_mfma_f32_32x32x16_bf16(pa2, PK(c2, d2), o1, 0, 0, 0);
;     o1 = __builtin_amdgcn_mfma_f32_32x32x16_bf16(pa3, PK(c3, d3), o1, 0, 0, 0);
;     ...
; }
; template <bool FIRST> DEVI bool partialSM(f32x16& p0, f32x16& p1, float& m_reg, float& alpha) {
;     float pmax = p0[0];
; #pragma unroll
;     for (int r = 1; r < 16; ++r) pmax = fmaxf(pmax, p0[r]);
; #pragma unroll
;     for (int r = 0; r < 16; ++r) pmax = fmaxf(pmax, p1[r]);
;     { auto rr = __builtin_amdgcn_permlane32_swap(__float_as_uint(pmax), __float_as_uint(pmax), false, false);
;       pmax = fmaxf(__uint_as_float(rr[0]), __uint_as_float(rr[1])); }
;     if (FIRST) { m_reg = pmax; alpha = 1.f;
; #pragma unroll
;         for (int r = 0; r < 16; ++r) { p0[r] = __builtin_amdgcn_exp2f(p0[r] - pmax); p1[r] = p1[r] - pmax; }
;         return false;
;     } else if (__builtin_expect(__all(pmax <= ATT_THR), 1)) { alpha = 1.f;
; #pragma unroll
;         for (int r = 0; r < 16; ++r) p0[r] = __builtin_amdgcn_exp2f(p0[r]);
;         return false;
;     } else { const float d = fmaxf(pmax, 0.f); alpha = __builtin_amdgcn_exp2f(-d); m_reg += d;
	v_exp_f32_e32 v58, v106
	v_exp_f32_e32 v59, v107
	v_permlane32_swap_b32_e32 v251, v252
	v_exp_f32_e32 v60, v108
	v_exp_f32_e32 v61, v109
	v_mfma_f32_32x32x16_bf16 v[18:33], v[62:65], v[78:81], v[18:33]
	v_mfma_f32_32x32x16_bf16 v[2:17], v[62:65], v[222:225], v[2:17]
	v_exp_f32_e32 v62, v110
	v_exp_f32_e32 v63, v111
	v_exp_f32_e32 v64, v112
	v_exp_f32_e32 v65, v113
	v_max_f32_e32 v252, v252, v252
	v_max_f32_e32 v251, v251, v251
	v_max_f32_e32 v126, v251, v252
	v_cmp_ge_f32_e32 vcc, s80, v126
	s_cmp_lg_u64 vcc, exec
	s_cselect_b64 s[6:7], -1, 0
	s_cbranch_scc1 .LBB0_2269
	v_mov_b32_e32 v209, 1.0

; DEVI void finishSM(f32x16& p0, f32x16& p1, float alpha, float& l_reg, bf16x8& pa0, bf16x8& pa1, bf16x8& pa2, bf16x8& pa3) {
; #pragma unroll
;     for (int r = 0; r < 16; ++r) p1[r] = __builtin_amdgcn_exp2f(p1[r]);
	v_exp_f32_e32 v82, v82
	v_exp_f32_e32 v83, v83
	v_exp_f32_e32 v84, v84
	v_exp_f32_e32 v85, v85
	v_exp_f32_e32 v86, v86
	v_exp_f32_e32 v87, v87
	v_exp_f32_e32 v88, v88
	v_exp_f32_e32 v89, v89
	v_exp_f32_e32 v90, v90
	v_exp_f32_e32 v91, v91
	v_exp_f32_e32 v92, v92
	v_exp_f32_e32 v93, v93
	v_exp_f32_e32 v94, v94
	v_exp_f32_e32 v95, v95
	v_exp_f32_e32 v96, v96
	v_exp_f32_e32 v97, v97
	s_branch .LBB0_2263

; DEVI void attn_unit8(const Params& p, char* smem, int unit, int l, int& cvs  , CvRun& crun) {
;     ...
;         const char* Kb = K_lds + s0 * 24576; const int vb = vb0 + s0 * 16384;
;         CvRegs cvr; cv_issue(p, l, cvs, lane, cvr, crun); cvs += (int)gridDim.x * 8;
;         qkt(pB0, pB1, Kb + 12288, qr, r32, hi, cinit);
.LBB0_2266:
	s_mul_i32 s98, s61, 0x6000
	s_add_i32 s98, s96, s98
	s_lshl_b32 s99, s61, 14
	s_add_i32 s99, s97, s99
	s_mul_i32 s6, s2, 0x6000
	s_add_i32 s6, s6, 0
	v_add_u32_e32 v249, s6, v129

; DEVI void qkt(f32x16& p0, f32x16& p1, const char* Kb, const bf16x8 (&qr)[6], int r32, int hi, const f32x16& cinit) {
; #pragma unroll
;     for (int d0 = 0; d0 < 6; ++d0) { const int cb = (d0 * 16 + hi * 8) * 2;
;         const bf16x8 k0 = *(const bf16x8*)(Kb + KSWZ(r32, cb)), k1 = *(const bf16x8*)(Kb + KSWZ(32 + r32, cb));
;         p0 = __builtin_amdgcn_mfma_f32_32x32x16_bf16(k0, qr[d0], d0 == 0 ? cinit : p0, 0, 0, 0);
;         p1 = __builtin_amdgcn_mfma_f32_32x32x16_bf16(k1, qr[d0], d0 == 0 ? cinit : p1, 0, 0, 0); }
	s_mov_b32 m0, s98
	s_barrier
	ds_read_b128 v[234:237], v249
	ds_read_b128 v[212:215], v249 offset:6144
	global_load_lds_dwordx4 v118, s[12:13]
	s_waitcnt lgkmcnt(0)
	v_mfma_f32_32x32x16_bf16 v[98:113], v[234:237], v[150:153], v[34:49]
	s_add_i32 m0, s98, 0x2000

; DEVI void qkt(f32x16& p0, f32x16& p1, const char* Kb, const bf16x8 (&qr)[6], int r32, int hi, const f32x16& cinit) {
; #pragma unroll
;     for (int d0 = 0; d0 < 6; ++d0) { const int cb = (d0 * 16 + hi * 8) * 2;
;         const bf16x8 k0 = *(const bf16x8*)(Kb + KSWZ(r32, cb)), k1 = *(const bf16x8*)(Kb + KSWZ(32 + r32, cb));
;         p0 = __builtin_amdgcn_mfma_f32_32x32x16_bf16(k0, qr[d0], d0 == 0 ? cinit : p0, 0, 0, 0);
;         p1 = __builtin_amdgcn_mfma_f32_32x32x16_bf16(k1, qr[d0], d0 == 0 ? cinit : p1, 0, 0, 0); }
	v_add_u32_e32 v126, s6, v184
	global_load_lds_dwordx4 v120, s[12:13]
	v_mfma_f32_32x32x16_bf16 v[66:81], v[212:215], v[150:153], v[34:49]
	ds_read_b128 v[212:215], v126
	ds_read_b128 v[216:219], v126 offset:6144
	s_add_i32 m0, s98, 0x4000

; DEVI void qkt(f32x16& p0, f32x16& p1, const char* Kb, const bf16x8 (&qr)[6], int r32, int hi, const f32x16& cinit) {
; #pragma unroll
;     for (int d0 = 0; d0 < 6; ++d0) { const int cb = (d0 * 16 + hi * 8) * 2;
;         const bf16x8 k0 = *(const bf16x8*)(Kb + KSWZ(r32, cb)), k1 = *(const bf16x8*)(Kb + KSWZ(32 + r32, cb));
;         p0 = __builtin_amdgcn_mfma_f32_32x32x16_bf16(k0, qr[d0], d0 == 0 ? cinit : p0, 0, 0, 0);
;         p1 = __builtin_amdgcn_mfma_f32_32x32x16_bf16(k1, qr[d0], d0 == 0 ? cinit : p1, 0, 0, 0); }
	v_add_u32_e32 v126, s6, v185
	global_load_lds_dwordx4 v122, s[12:13]
	s_mov_b32 m0, s99
	s_waitcnt lgkmcnt(0)
	v_mfma_f32_32x32x16_bf16 v[98:113], v[212:215], v[138:141], v[98:113]


	global_load_lds_dwordx4 v116, s[44:45]
	s_add_i32 m0, s99, 0x2000


; template <int OFF> DEVI s16x4 tr_read(int vb) { s16x4 r; asm volatile("ds_read_b64_tr_b16 %0, %1 offset:%2" : "=&v"(r) : "v"(vb), "i"(OFF) : "memory"); return r; }
; DEVI void pv_both(f32x16& o0, f32x16& o1, int vb, bf16x8 pa0, bf16x8 pa1, bf16x8 pa2, bf16x8 pa3) {
;     const s16x4 a0 = tr_read<v_rd_off(0, 0, 0)>(vb), b0 = tr_read<v_rd_off(0, 0, 1)>(vb), a1 = tr_read<v_rd_off(0, 1, 0)>(vb), b1 = tr_read<v_rd_off(0, 1, 1)>(vb);
;     const s16x4 a2 = tr_read<v_rd_off(0, 2, 0)>(vb), b2 = tr_read<v_rd_off(0, 2, 1)>(vb), a3 = tr_read<v_rd_off(0, 3, 0)>(vb), b3 = tr_read<v_rd_off(0, 3, 1)>(vb);
;     const s16x4 c0 = tr_read<v_rd_off(1, 0, 0)>(vb), d0 = tr_read<v_rd_off(1, 0, 1)>(vb), c1 = tr_read<v_rd_off(1, 1, 0)>(vb), d1 = tr_read<v_rd_off(1, 1, 1)>(vb);
;     const s16x4 c2 = tr_read<v_rd_off(1, 2, 0)>(vb), d2 = tr_read<v_rd_off(1, 2, 1)>(vb), c3 = tr_read<v_rd_off(1, 3, 0)>(vb), d3 = tr_read<v_rd_off(1, 3, 1)>(vb);
; DEVI void finishSM(f32x16& p0, f32x16& p1, float alpha, float& l_reg, bf16x8& pa0, bf16x8& pa1, bf16x8& pa2, bf16x8& pa3) {
; #pragma unroll
;     for (int r = 0; r < 16; ++r) p1[r] = __builtin_amdgcn_exp2f(p1[r]);
;     f32x2 s2 = (f32x2){p0[0], p0[1]} + (f32x2){p1[0], p1[1]};
; #pragma unroll
;     for (int r = 2; r < 16; r += 2) s2 += (f32x2){p0[r], p0[r + 1]} + (f32x2){p1[r], p1[r + 1]};
;     float ps = s2[0] + s2[1];
;     { auto rr = __builtin_amdgcn_permlane32_swap(__float_as_uint(ps), __float_as_uint(ps), false, false);
;       ps = __uint_as_float(rr[0]) + __uint_as_float(rr[1]); }
;     l_reg = l_reg * alpha + ps;
;     ...
;     PK4(p0, 0, pa0); PK4(p0, 8, pa1); PK4(p1, 0, pa2); PK4(p1, 8, pa3);
;     ...
; }
; DEVI void qkt(f32x16& p0, f32x16& p1, const char* Kb, const bf16x8 (&qr)[6], int r32, int hi, const f32x16& cinit) {
; #pragma unroll
;     for (int d0 = 0; d0 < 6; ++d0) { const int cb = (d0 * 16 + hi * 8) * 2;
;         const bf16x8 k0 = *(const bf16x8*)(Kb + KSWZ(r32, cb)), k1 = *(const bf16x8*)(Kb + KSWZ(32 + r32, cb));
;         p0 = __builtin_amdgcn_mfma_f32_32x32x16_bf16(k0, qr[d0], d0 == 0 ? cinit : p0, 0, 0, 0);
;         p1 = __builtin_amdgcn_mfma_f32_32x32x16_bf16(k1, qr[d0], d0 == 0 ? cinit : p1, 0, 0, 0); }
	v_mfma_f32_32x32x16_bf16 v[66:81], v[216:219], v[138:141], v[66:81]
	global_load_lds_dwordx4 v117, s[44:45]
	ds_read_b128 v[212:215], v126
	ds_read_b128 v[216:219], v126 offset:6144
	v_add_u32_e32 v126, s6, v205
	s_waitcnt lgkmcnt(1)
	v_mfma_f32_32x32x16_bf16 v[98:113], v[212:215], v[134:137], v[98:113]
	ds_read_b128 v[212:215], v126
	ds_read_b128 v[220:223], v126 offset:6144
	v_add_u32_e32 v126, s6, v206
	s_waitcnt lgkmcnt(2)
	v_mfma_f32_32x32x16_bf16 v[66:81], v[216:219], v[134:137], v[66:81]
	ds_read_b128 v[216:219], v126
	ds_read_b128 v[224:227], v126 offset:6144
	v_add_u32_e32 v126, s6, v207
	ds_read_b128 v[228:231], v126
	ds_read_b128 v[232:235], v126 offset:6144
	v_add_f32_e32 v126, v50, v82
	v_add_f32_e32 v127, v51, v83
	v_cvt_pk_bf16_f32 v50, v50, v51
	v_cvt_pk_bf16_f32 v51, v52, v53
	s_waitcnt lgkmcnt(2)
	v_mfma_f32_32x32x16_bf16 v[98:113], v[212:215], v[130:133], v[98:113]
	v_add_f32_e64 v212, v52, v84
	v_add_f32_e64 v213, v53, v85
	v_cvt_pk_bf16_f32 v52, v54, v55
	v_cvt_pk_bf16_f32 v53, v56, v57
	v_add_f32_e64 v126, v212, v126
	v_add_f32_e64 v127, v213, v127
	v_add_f32_e64 v212, v54, v86
	v_add_f32_e64 v213, v55, v87
	v_cvt_pk_bf16_f32 v54, v58, v59
	v_mfma_f32_32x32x16_bf16 v[66:81], v[220:223], v[130:133], v[66:81]
	v_add_f32_e64 v126, v212, v126
	v_add_f32_e64 v127, v213, v127
	v_add_f32_e64 v212, v56, v88
	v_add_f32_e64 v213, v57, v89
	v_cvt_pk_bf16_f32 v55, v60, v61
	v_cvt_pk_bf16_f32 v56, v62, v63
	v_cvt_pk_bf16_f32 v57, v64, v65
	v_add_f32_e64 v126, v212, v126
	v_add_f32_e64 v127, v213, v127
	v_add_f32_e32 v212, v58, v90
	v_add_f32_e32 v213, v59, v91
	v_cvt_pk_bf16_f32 v58, v82, v83
	v_cvt_pk_bf16_f32 v59, v84, v85
	v_mfma_f32_32x32x16_bf16 v[98:113], v[216:219], v[146:149], v[98:113]
	v_add_f32_e64 v126, v212, v126
	v_add_f32_e64 v127, v213, v127
	v_add_f32_e64 v212, v60, v92
	v_add_f32_e64 v213, v61, v93
	v_cvt_pk_bf16_f32 v60, v86, v87
	v_cvt_pk_bf16_f32 v61, v88, v89
	v_add_f32_e64 v126, v212, v126
	v_add_f32_e64 v127, v213, v127
	v_add_f32_e32 v212, v62, v94
	v_add_f32_e32 v213, v63, v95
	v_cvt_pk_bf16_f32 v62, v90, v91
	v_cvt_pk_bf16_f32 v63, v92, v93
	v_mfma_f32_32x32x16_bf16 v[66:81], v[224:227], v[146:149], v[66:81]
	v_add_f32_e64 v126, v212, v126
	v_add_f32_e64 v127, v213, v127
	v_add_f32_e64 v212, v64, v96
	v_add_f32_e64 v213, v65, v97
	v_cvt_pk_bf16_f32 v64, v94, v95
	v_cvt_pk_bf16_f32 v65, v96, v97
	ds_read_b64_tr_b16 v[154:155], v203 offset:0x2000
	ds_read_b64_tr_b16 v[156:157], v203 offset:0x2400
	ds_read_b64_tr_b16 v[158:159], v203 offset:0x2800
	ds_read_b64_tr_b16 v[160:161], v203 offset:0x2c00
	ds_read_b64_tr_b16 v[162:163], v203 offset:0x3000
	ds_read_b64_tr_b16 v[164:165], v203 offset:0x3400
	ds_read_b64_tr_b16 v[166:167], v203 offset:0x3800
	ds_read_b64_tr_b16 v[168:169], v203 offset:0x3c00
	v_add_f32_e64 v126, v212, v126
	v_add_f32_e64 v127, v213, v127
	ds_read_b64_tr_b16 v[212:213], v203 offset:0x2200
	ds_read_b64_tr_b16 v[214:215], v203 offset:0x2600
	ds_read_b64_tr_b16 v[216:217], v203 offset:0x2a00
	s_waitcnt lgkmcnt(12)
	v_mfma_f32_32x32x16_bf16 v[98:113], v[228:231], v[142:145], v[98:113]
	ds_read_b64_tr_b16 v[218:219], v203 offset:0x2e00
	ds_read_b64_tr_b16 v[220:221], v203 offset:0x3200
	ds_read_b64_tr_b16 v[222:223], v203 offset:0x3600
	ds_read_b64_tr_b16 v[224:225], v203 offset:0x3a00
	ds_read_b64_tr_b16 v[226:227], v203 offset:0x3e00
	v_add_f32_e32 v126, v126, v127
	s_waitcnt lgkmcnt(6)
	v_mfma_f32_32x32x16_bf16 v[66:81], v[232:235], v[142:145], v[66:81]
	v_mov_b32_e32 v127, v126


; #define SBAR() __builtin_amdgcn_sched_barrier(0)
; DEVI void pv_both(f32x16& o0, f32x16& o1, int vb, bf16x8 pa0, bf16x8 pa1, bf16x8 pa2, bf16x8 pa3) {
;     ...
;     o0 = __builtin_amdgcn_mfma_f32_32x32x16_bf16(pa0, PK(a0, b0), o0, 0, 0, 0);
;     o0 = __builtin_amdgcn_mfma_f32_32x32x16_bf16(pa1, PK(a1, b1), o0, 0, 0, 0);
;     o0 = __builtin_amdgcn_mfma_f32_32x32x16_bf16(pa2, PK(a2, b2), o0, 0, 0, 0);
;     o0 = __builtin_amdgcn_mfma_f32_32x32x16_bf16(pa3, PK(a3, b3), o0, 0, 0, 0);
;     asm volatile("s_waitcnt lgkmcnt(0)" ::: "memory"); SBAR();
;     o1 = __builtin_amdgcn_mfma_f32_32x32x16_bf16(pa0, PK(c0, d0), o1, 0, 0, 0);
;     o1 = __builtin_amdgcn_mfma_f32_32x32x16_bf16(pa1, PK(c1, d1), o1, 0, 0, 0);
;     o1 = __builtin_amdgcn_mfma_f32_32x32x16_bf16(pa2, PK(c2, d2), o1, 0, 0, 0);
;     o1 = __builtin_amdgcn_mfma_f32_32x32x16_bf16(pa3, PK(c3, d3), o1, 0, 0, 0);
;     ...
; }
; template <bool FIRST> DEVI bool partialSM(f32x16& p0, f32x16& p1, float& m_reg, float& alpha) {
;     float pmax = p0[0];
; #pragma unroll
;     for (int r = 1; r < 16; ++r) pmax = fmaxf(pmax, p0[r]);
; #pragma unroll
;     for (int r = 0; r < 16; ++r) pmax = fmaxf(pmax, p1[r]);
;     { auto rr = __builtin_amdgcn_permlane32_swap(__float_as_uint(pmax), __float_as_uint(pmax), false, false);
;       pmax = fmaxf(__uint_as_float(rr[0]), __uint_as_float(rr[1])); }
;     if (FIRST) { m_reg = pmax; alpha = 1.f;
; #pragma unroll
;         for (int r = 0; r < 16; ++r) { p0[r] = __builtin_amdgcn_exp2f(p0[r] - pmax); p1[r] = p1[r] - pmax; }
;         return false;
;     } else if (__builtin_expect(__all(pmax <= ATT_THR), 1)) { alpha = 1.f;
; #pragma unroll
;         for (int r = 0; r < 16; ++r) p0[r] = __builtin_amdgcn_exp2f(p0[r]);
	v_mfma_f32_32x32x16_bf16 v[18:33], v[50:53], v[154:157], v[18:33]
	v_permlane32_swap_b32_e32 v126, v127
	v_mfma_f32_32x32x16_bf16 v[2:17], v[50:53], v[212:215], v[2:17]
	s_nop 1
	v_max_f32_e32 v249, v99, v99
	v_max_f32_e32 v250, v98, v98
	v_max_f32_e32 v249, v250, v249
	v_max3_f32 v249, v249, v100, v101
	v_max3_f32 v249, v249, v102, v103
	v_max3_f32 v251, v249, v104, v105
	v_max3_f32 v251, v251, v106, v107
	v_exp_f32_e32 v50, v98
	v_exp_f32_e32 v51, v99
	v_exp_f32_e32 v52, v100
	v_exp_f32_e32 v53, v101
	v_mfma_f32_32x32x16_bf16 v[18:33], v[54:57], v[158:161], v[18:33]
	s_waitcnt lgkmcnt(2)
	v_mfma_f32_32x32x16_bf16 v[2:17], v[54:57], v[216:219], v[2:17]
	v_max3_f32 v251, v251, v108, v109
	v_max3_f32 v251, v251, v110, v111
	v_max3_f32 v251, v251, v112, v113
	v_max3_f32 v251, v251, v66, v67
	v_max3_f32 v251, v251, v68, v69
	v_max3_f32 v251, v251, v70, v71
	v_max3_f32 v251, v251, v72, v73
	v_exp_f32_e32 v54, v102
	v_exp_f32_e32 v55, v103
	v_exp_f32_e32 v56, v104
	v_exp_f32_e32 v57, v105
	v_mfma_f32_32x32x16_bf16 v[18:33], v[58:61], v[162:165], v[18:33]
	v_mfma_f32_32x32x16_bf16 v[2:17], v[58:61], v[220:223], v[2:17]
	v_max3_f32 v251, v251, v74, v75
	v_max3_f32 v251, v251, v76, v77
	v_max3_f32 v251, v251, v78, v79
	v_max3_f32 v251, v251, v80, v81
	v_mov_b32_e32 v252, v251


; DEVI void pv_both(f32x16& o0, f32x16& o1, int vb, bf16x8 pa0, bf16x8 pa1, bf16x8 pa2, bf16x8 pa3) {
;     ...
;     o1 = __builtin_amdgcn_mfma_f32_32x32x16_bf16(pa1, PK(c1, d1), o1, 0, 0, 0);
;     o1 = __builtin_amdgcn_mfma_f32_32x32x16_bf16(pa2, PK(c2, d2), o1, 0, 0, 0);
;     o1 = __builtin_amdgcn_mfma_f32_32x32x16_bf16(pa3, PK(c3, d3), o1, 0, 0, 0);
;     ...
; }
; template <bool FIRST> DEVI bool partialSM(f32x16& p0, f32x16& p1, float& m_reg, float& alpha) {
;     float pmax = p0[0];
; #pragma unroll
;     for (int r = 1; r < 16; ++r) pmax = fmaxf(pmax, p0[r]);
; #pragma unroll
;     for (int r = 0; r < 16; ++r) pmax = fmaxf(pmax, p1[r]);
;     { auto rr = __builtin_amdgcn_permlane32_swap(__float_as_uint(pmax), __float_as_uint(pmax), false, false);
;       pmax = fmaxf(__uint_as_float(rr[0]), __uint_as_float(rr[1])); }
;     if (FIRST) { m_reg = pmax; alpha = 1.f;
; #pragma unroll
;         for (int r = 0; r < 16; ++r) { p0[r] = __builtin_amdgcn_exp2f(p0[r] - pmax); p1[r] = p1[r] - pmax; }
;         return false;
;     } else if (__builtin_expect(__all(pmax <= ATT_THR), 1)) { alpha = 1.f;
; #pragma unroll
;         for (int r = 0; r < 16; ++r) p0[r] = __builtin_amdgcn_exp2f(p0[r]);
;         return false;
;     } else { const float d = fmaxf(pmax, 0.f); alpha = __builtin_amdgcn_exp2f(-d); m_reg += d;
	v_exp_f32_e32 v58, v106
	v_exp_f32_e32 v59, v107
	v_permlane32_swap_b32_e32 v251, v252
	v_exp_f32_e32 v60, v108
	v_exp_f32_e32 v61, v109
	v_mfma_f32_32x32x16_bf16 v[18:33], v[62:65], v[166:169], v[18:33]
	s_waitcnt lgkmcnt(0)
	v_mfma_f32_32x32x16_bf16 v[2:17], v[62:65], v[224:227], v[2:17]
	v_exp_f32_e32 v62, v110
	v_exp_f32_e32 v63, v111
	v_exp_f32_e32 v64, v112
	v_exp_f32_e32 v65, v113
	v_max_f32_e32 v252, v252, v252
	v_max_f32_e32 v251, v251, v251
	v_max_f32_e32 v174, v251, v252
	v_cmp_ge_f32_e32 vcc, s80, v174
	s_cmp_lg_u64 vcc, exec
	s_cselect_b64 s[6:7], -1, 0
	s_cbranch_scc1 .LBB0_2275
	v_mov_b32_e32 v203, 1.0

; template <bool FIRST> DEVI bool partialSM(f32x16& p0, f32x16& p1, float& m_reg, float& alpha) {
;     ...
;     } else if (__builtin_expect(__all(pmax <= ATT_THR), 1)) { alpha = 1.f;
; #pragma unroll
;         for (int r = 0; r < 16; ++r) p0[r] = __builtin_amdgcn_exp2f(p0[r]);
;         return false;
	s_branch .LBB0_2280
